# cache-policy hints: k_l2 record loads plain instead of nt; last-layer epilogue once-read rows (x1, x2/x3 tables, ego row) loaded nt
# speedup vs baseline: 1.0825x; 1.0074x over previous
.LBB3_46:
	s_and_b64 vcc, exec, s[0:1]
	s_cbranch_vccz .LBB3_141
	s_ashr_i32 s37, s36, 31
	s_lshl_b64 s[0:1], s[36:37], 3
	s_add_u32 s0, s2, s0
	s_addc_u32 s1, s3, s1
	s_add_i32 s8, s44, 31
	s_lshr_b32 s8, s8, 5
	s_add_i32 s8, s8, -1
	s_lshl_b32 s9, s42, 2
	s_sub_i32 s8, s8, s9
	s_bfe_u32 s8, s8, 0x1000a
	s_mul_i32 s8, s8, 31
	v_mov_b32_e32 v50, 0
	v_mov_b32_e32 v51, 0
	v_mov_b32_e32 v52, 0
	v_mov_b32_e32 v53, 0
	v_lshlrev_b32_e32 v1, 4, v0
	ds_write_b128 v1, v[50:53]
	v_mov_b32_e32 v63, 1
	v_add_u32_e32 v54, 0, v0
	v_lshl_add_u32 v54, v54, 1, 0
	v_cmp_gt_i32_e32 vcc, s33, v54
	v_lshlrev_b32_e32 v54, 3, v54
	s_and_saveexec_b64 s[4:5], vcc
	global_load_dwordx4 v[2:5], v54, s[0:1]
	s_or_b64 exec, exec, s[4:5]
	v_add_u32_e32 v54, 1024, v0
	v_lshl_add_u32 v54, v54, 1, 0
	v_cmp_gt_i32_e32 vcc, s33, v54
	v_lshlrev_b32_e32 v54, 3, v54
	s_and_saveexec_b64 s[4:5], vcc
	global_load_dwordx4 v[6:9], v54, s[0:1]
	s_or_b64 exec, exec, s[4:5]
	v_add_u32_e32 v54, 2048, v0
	v_lshl_add_u32 v54, v54, 1, 0
	v_cmp_gt_i32_e32 vcc, s33, v54
	v_lshlrev_b32_e32 v54, 3, v54
	s_and_saveexec_b64 s[4:5], vcc
	global_load_dwordx4 v[10:13], v54, s[0:1]
	s_or_b64 exec, exec, s[4:5]
	v_add_u32_e32 v54, 3072, v0
	v_lshl_add_u32 v54, v54, 1, 0
	v_cmp_gt_i32_e32 vcc, s33, v54
	v_lshlrev_b32_e32 v54, 3, v54
	s_and_saveexec_b64 s[4:5], vcc
	global_load_dwordx4 v[14:17], v54, s[0:1]
	s_or_b64 exec, exec, s[4:5]
	v_add_u32_e32 v54, 4096, v0
	v_lshl_add_u32 v54, v54, 1, 0
	v_cmp_gt_i32_e32 vcc, s33, v54
	v_lshlrev_b32_e32 v54, 3, v54
	s_and_saveexec_b64 s[4:5], vcc
	global_load_dwordx4 v[18:21], v54, s[0:1]
	s_or_b64 exec, exec, s[4:5]
	v_add_u32_e32 v54, 5120, v0
	v_lshl_add_u32 v54, v54, 1, 0
	v_cmp_gt_i32_e32 vcc, s33, v54
	v_lshlrev_b32_e32 v54, 3, v54
	s_and_saveexec_b64 s[4:5], vcc
	global_load_dwordx4 v[22:25], v54, s[0:1]
	s_or_b64 exec, exec, s[4:5]
	v_add_u32_e32 v54, 6144, v0
	v_lshl_add_u32 v54, v54, 1, 0
	v_cmp_gt_i32_e32 vcc, s33, v54
	v_lshlrev_b32_e32 v54, 3, v54
	s_and_saveexec_b64 s[4:5], vcc
	global_load_dwordx4 v[26:29], v54, s[0:1]
	s_or_b64 exec, exec, s[4:5]
	v_add_u32_e32 v54, 7168, v0
	v_lshl_add_u32 v54, v54, 1, 0
	v_cmp_gt_i32_e32 vcc, s33, v54
	v_lshlrev_b32_e32 v54, 3, v54
	s_and_saveexec_b64 s[4:5], vcc
	global_load_dwordx4 v[30:33], v54, s[0:1]
	s_or_b64 exec, exec, s[4:5]
	s_waitcnt lgkmcnt(0)
	s_barrier
	s_waitcnt vmcnt(7)
	v_lshrrev_b32_e32 v54, 25, v2
	v_bfe_u32 v55, v2, 13, 12
	v_min_u32_e32 v55, 31, v55
	v_xor_b32_e32 v55, s8, v55
	v_lshl_or_b32 v54, v54, 5, v55
	v_lshlrev_b32_e32 v56, 2, v54
	v_add_u32_e32 v54, 0, v0
	v_lshl_add_u32 v54, v54, 1, 0
	v_cmp_gt_i32_e32 vcc, s33, v54
	s_and_saveexec_b64 s[4:5], vcc
	ds_add_rtn_u32 v34, v56, v63
	s_or_b64 exec, exec, s[4:5]
	s_waitcnt vmcnt(7)
	v_lshrrev_b32_e32 v54, 25, v4
	v_bfe_u32 v55, v4, 13, 12
	v_min_u32_e32 v55, 31, v55
	v_xor_b32_e32 v55, s8, v55
	v_lshl_or_b32 v54, v54, 5, v55
	v_lshlrev_b32_e32 v56, 2, v54
	v_add_u32_e32 v54, 0, v0
	v_lshl_add_u32 v54, v54, 1, 1
	v_cmp_gt_i32_e32 vcc, s33, v54
	s_and_saveexec_b64 s[4:5], vcc
	ds_add_rtn_u32 v35, v56, v63
	s_or_b64 exec, exec, s[4:5]
	s_waitcnt vmcnt(6)
	v_lshrrev_b32_e32 v54, 25, v6
	v_bfe_u32 v55, v6, 13, 12
	v_min_u32_e32 v55, 31, v55
	v_xor_b32_e32 v55, s8, v55
	v_lshl_or_b32 v54, v54, 5, v55
	v_lshlrev_b32_e32 v56, 2, v54
	v_add_u32_e32 v54, 1024, v0
	v_lshl_add_u32 v54, v54, 1, 0
	v_cmp_gt_i32_e32 vcc, s33, v54
	s_and_saveexec_b64 s[4:5], vcc
	ds_add_rtn_u32 v36, v56, v63
	s_or_b64 exec, exec, s[4:5]
	s_waitcnt vmcnt(6)
	v_lshrrev_b32_e32 v54, 25, v8
	v_bfe_u32 v55, v8, 13, 12
	v_min_u32_e32 v55, 31, v55
	v_xor_b32_e32 v55, s8, v55
	v_lshl_or_b32 v54, v54, 5, v55
	v_lshlrev_b32_e32 v56, 2, v54
	v_add_u32_e32 v54, 1024, v0
	v_lshl_add_u32 v54, v54, 1, 1
	v_cmp_gt_i32_e32 vcc, s33, v54
	s_and_saveexec_b64 s[4:5], vcc
	ds_add_rtn_u32 v37, v56, v63
	s_or_b64 exec, exec, s[4:5]
	s_waitcnt vmcnt(5)
	v_lshrrev_b32_e32 v54, 25, v10
	v_bfe_u32 v55, v10, 13, 12
	v_min_u32_e32 v55, 31, v55
	v_xor_b32_e32 v55, s8, v55
	v_lshl_or_b32 v54, v54, 5, v55
	v_lshlrev_b32_e32 v56, 2, v54
	v_add_u32_e32 v54, 2048, v0
	v_lshl_add_u32 v54, v54, 1, 0
	v_cmp_gt_i32_e32 vcc, s33, v54
	s_and_saveexec_b64 s[4:5], vcc
	ds_add_rtn_u32 v38, v56, v63
	s_or_b64 exec, exec, s[4:5]
	s_waitcnt vmcnt(5)
	v_lshrrev_b32_e32 v54, 25, v12
	v_bfe_u32 v55, v12, 13, 12
	v_min_u32_e32 v55, 31, v55
	v_xor_b32_e32 v55, s8, v55
	v_lshl_or_b32 v54, v54, 5, v55
	v_lshlrev_b32_e32 v56, 2, v54
	v_add_u32_e32 v54, 2048, v0
	v_lshl_add_u32 v54, v54, 1, 1
	v_cmp_gt_i32_e32 vcc, s33, v54
	s_and_saveexec_b64 s[4:5], vcc
	ds_add_rtn_u32 v39, v56, v63
	s_or_b64 exec, exec, s[4:5]
	s_waitcnt vmcnt(4)
	v_lshrrev_b32_e32 v54, 25, v14
	v_bfe_u32 v55, v14, 13, 12
	v_min_u32_e32 v55, 31, v55
	v_xor_b32_e32 v55, s8, v55
	v_lshl_or_b32 v54, v54, 5, v55
	v_lshlrev_b32_e32 v56, 2, v54
	v_add_u32_e32 v54, 3072, v0
	v_lshl_add_u32 v54, v54, 1, 0
	v_cmp_gt_i32_e32 vcc, s33, v54
	s_and_saveexec_b64 s[4:5], vcc
	ds_add_rtn_u32 v40, v56, v63
	s_or_b64 exec, exec, s[4:5]
	s_waitcnt vmcnt(4)
	v_lshrrev_b32_e32 v54, 25, v16
	v_bfe_u32 v55, v16, 13, 12
	v_min_u32_e32 v55, 31, v55
	v_xor_b32_e32 v55, s8, v55
	v_lshl_or_b32 v54, v54, 5, v55
	v_lshlrev_b32_e32 v56, 2, v54
	v_add_u32_e32 v54, 3072, v0
	v_lshl_add_u32 v54, v54, 1, 1
	v_cmp_gt_i32_e32 vcc, s33, v54
	s_and_saveexec_b64 s[4:5], vcc
	ds_add_rtn_u32 v41, v56, v63
	s_or_b64 exec, exec, s[4:5]
	s_waitcnt vmcnt(3)
	v_lshrrev_b32_e32 v54, 25, v18
	v_bfe_u32 v55, v18, 13, 12
	v_min_u32_e32 v55, 31, v55
	v_xor_b32_e32 v55, s8, v55
	v_lshl_or_b32 v54, v54, 5, v55
	v_lshlrev_b32_e32 v56, 2, v54
	v_add_u32_e32 v54, 4096, v0
	v_lshl_add_u32 v54, v54, 1, 0
	v_cmp_gt_i32_e32 vcc, s33, v54
	s_and_saveexec_b64 s[4:5], vcc
	ds_add_rtn_u32 v42, v56, v63
	s_or_b64 exec, exec, s[4:5]
	s_waitcnt vmcnt(3)
	v_lshrrev_b32_e32 v54, 25, v20
	v_bfe_u32 v55, v20, 13, 12
	v_min_u32_e32 v55, 31, v55
	v_xor_b32_e32 v55, s8, v55
	v_lshl_or_b32 v54, v54, 5, v55
	v_lshlrev_b32_e32 v56, 2, v54
	v_add_u32_e32 v54, 4096, v0
	v_lshl_add_u32 v54, v54, 1, 1
	v_cmp_gt_i32_e32 vcc, s33, v54
	s_and_saveexec_b64 s[4:5], vcc
	ds_add_rtn_u32 v43, v56, v63
	s_or_b64 exec, exec, s[4:5]
	s_waitcnt vmcnt(2)
	v_lshrrev_b32_e32 v54, 25, v22
	v_bfe_u32 v55, v22, 13, 12
	v_min_u32_e32 v55, 31, v55
	v_xor_b32_e32 v55, s8, v55
	v_lshl_or_b32 v54, v54, 5, v55
	v_lshlrev_b32_e32 v56, 2, v54
	v_add_u32_e32 v54, 5120, v0
	v_lshl_add_u32 v54, v54, 1, 0
	v_cmp_gt_i32_e32 vcc, s33, v54
	s_and_saveexec_b64 s[4:5], vcc
	ds_add_rtn_u32 v44, v56, v63
	s_or_b64 exec, exec, s[4:5]
	s_waitcnt vmcnt(2)
	v_lshrrev_b32_e32 v54, 25, v24
	v_bfe_u32 v55, v24, 13, 12
	v_min_u32_e32 v55, 31, v55
	v_xor_b32_e32 v55, s8, v55
	v_lshl_or_b32 v54, v54, 5, v55
	v_lshlrev_b32_e32 v56, 2, v54
	v_add_u32_e32 v54, 5120, v0
	v_lshl_add_u32 v54, v54, 1, 1
	v_cmp_gt_i32_e32 vcc, s33, v54
	s_and_saveexec_b64 s[4:5], vcc
	ds_add_rtn_u32 v45, v56, v63
	s_or_b64 exec, exec, s[4:5]
	s_waitcnt vmcnt(1)
	v_lshrrev_b32_e32 v54, 25, v26
	v_bfe_u32 v55, v26, 13, 12
	v_min_u32_e32 v55, 31, v55
	v_xor_b32_e32 v55, s8, v55
	v_lshl_or_b32 v54, v54, 5, v55
	v_lshlrev_b32_e32 v56, 2, v54
	v_add_u32_e32 v54, 6144, v0
	v_lshl_add_u32 v54, v54, 1, 0
	v_cmp_gt_i32_e32 vcc, s33, v54
	s_and_saveexec_b64 s[4:5], vcc
	ds_add_rtn_u32 v46, v56, v63
	s_or_b64 exec, exec, s[4:5]
	s_waitcnt vmcnt(1)
	v_lshrrev_b32_e32 v54, 25, v28
	v_bfe_u32 v55, v28, 13, 12
	v_min_u32_e32 v55, 31, v55
	v_xor_b32_e32 v55, s8, v55
	v_lshl_or_b32 v54, v54, 5, v55
	v_lshlrev_b32_e32 v56, 2, v54
	v_add_u32_e32 v54, 6144, v0
	v_lshl_add_u32 v54, v54, 1, 1
	v_cmp_gt_i32_e32 vcc, s33, v54
	s_and_saveexec_b64 s[4:5], vcc
	ds_add_rtn_u32 v47, v56, v63
	s_or_b64 exec, exec, s[4:5]
	s_waitcnt vmcnt(0)
	v_lshrrev_b32_e32 v54, 25, v30
	v_bfe_u32 v55, v30, 13, 12
	v_min_u32_e32 v55, 31, v55
	v_xor_b32_e32 v55, s8, v55
	v_lshl_or_b32 v54, v54, 5, v55
	v_lshlrev_b32_e32 v56, 2, v54
	v_add_u32_e32 v54, 7168, v0
	v_lshl_add_u32 v54, v54, 1, 0
	v_cmp_gt_i32_e32 vcc, s33, v54
	s_and_saveexec_b64 s[4:5], vcc
	ds_add_rtn_u32 v48, v56, v63
	s_or_b64 exec, exec, s[4:5]
	s_waitcnt vmcnt(0)
	v_lshrrev_b32_e32 v54, 25, v32
	v_bfe_u32 v55, v32, 13, 12
	v_min_u32_e32 v55, 31, v55
	v_xor_b32_e32 v55, s8, v55
	v_lshl_or_b32 v54, v54, 5, v55
	v_lshlrev_b32_e32 v56, 2, v54
	v_add_u32_e32 v54, 7168, v0
	v_lshl_add_u32 v54, v54, 1, 1
	v_cmp_gt_i32_e32 vcc, s33, v54
	s_and_saveexec_b64 s[4:5], vcc
	ds_add_rtn_u32 v49, v56, v63
	s_or_b64 exec, exec, s[4:5]
	s_waitcnt lgkmcnt(0)
	s_barrier
	ds_read_b128 v[50:53], v1
	v_mbcnt_lo_u32_b32 v54, -1, 0
	v_mbcnt_hi_u32_b32 v54, -1, v54
	v_lshrrev_b32_e32 v55, 6, v0
	s_waitcnt lgkmcnt(0)
	v_add_u32_e32 v56, v50, v51
	v_add_u32_e32 v57, v56, v52
	v_add_u32_e32 v58, v57, v53
	v_mov_b32_e32 v59, v58
	v_subrev_u32_e32 v61, 1, v54
	v_lshlrev_b32_e32 v61, 2, v61
	ds_bpermute_b32 v60, v61, v59
	v_cmp_le_u32_e32 vcc, 1, v54
	s_waitcnt lgkmcnt(0)
	v_cndmask_b32_e32 v60, 0, v60, vcc
	v_add_u32_e32 v59, v59, v60
	v_subrev_u32_e32 v61, 2, v54
	v_lshlrev_b32_e32 v61, 2, v61
	ds_bpermute_b32 v60, v61, v59
	v_cmp_le_u32_e32 vcc, 2, v54
	s_waitcnt lgkmcnt(0)
	v_cndmask_b32_e32 v60, 0, v60, vcc
	v_add_u32_e32 v59, v59, v60
	v_subrev_u32_e32 v61, 4, v54
	v_lshlrev_b32_e32 v61, 2, v61
	ds_bpermute_b32 v60, v61, v59
	v_cmp_le_u32_e32 vcc, 4, v54
	s_waitcnt lgkmcnt(0)
	v_cndmask_b32_e32 v60, 0, v60, vcc
	v_add_u32_e32 v59, v59, v60
	v_subrev_u32_e32 v61, 8, v54
	v_lshlrev_b32_e32 v61, 2, v61
	ds_bpermute_b32 v60, v61, v59
	v_cmp_le_u32_e32 vcc, 8, v54
	s_waitcnt lgkmcnt(0)
	v_cndmask_b32_e32 v60, 0, v60, vcc
	v_add_u32_e32 v59, v59, v60
	v_subrev_u32_e32 v61, 16, v54
	v_lshlrev_b32_e32 v61, 2, v61
	ds_bpermute_b32 v60, v61, v59
	v_cmp_le_u32_e32 vcc, 16, v54
	s_waitcnt lgkmcnt(0)
	v_cndmask_b32_e32 v60, 0, v60, vcc
	v_add_u32_e32 v59, v59, v60
	v_subrev_u32_e32 v61, 32, v54
	v_lshlrev_b32_e32 v61, 2, v61
	ds_bpermute_b32 v60, v61, v59
	v_cmp_le_u32_e32 vcc, 32, v54
	s_waitcnt lgkmcnt(0)
	v_cndmask_b32_e32 v60, 0, v60, vcc
	v_add_u32_e32 v59, v59, v60
	v_lshlrev_b32_e32 v61, 2, v55
	v_cmp_eq_u32_e32 vcc, 63, v54
	s_and_saveexec_b64 s[4:5], vcc
	ds_write_b32 v61, v59 offset:16384
	s_or_b64 exec, exec, s[4:5]
	s_waitcnt lgkmcnt(0)
	s_barrier
	v_mov_b32_e32 v54, 0
	v_mov_b32_e32 v61, 0
	ds_read_b128 v[60:63], v61 offset:16384
	s_waitcnt lgkmcnt(0)
	v_cmp_lt_u32_e32 vcc, 0, v55
	s_nop 1
	v_cndmask_b32_e32 v60, 0, v60, vcc
	v_add_u32_e32 v54, v54, v60
	v_cmp_lt_u32_e32 vcc, 1, v55
	s_nop 1
	v_cndmask_b32_e32 v61, 0, v61, vcc
	v_add_u32_e32 v54, v54, v61
	v_cmp_lt_u32_e32 vcc, 2, v55
	s_nop 1
	v_cndmask_b32_e32 v62, 0, v62, vcc
	v_add_u32_e32 v54, v54, v62
	v_cmp_lt_u32_e32 vcc, 3, v55
	s_nop 1
	v_cndmask_b32_e32 v63, 0, v63, vcc
	v_add_u32_e32 v54, v54, v63
	v_mov_b32_e32 v61, 0
	ds_read_b128 v[60:63], v61 offset:16400
	s_waitcnt lgkmcnt(0)
	v_cmp_lt_u32_e32 vcc, 4, v55
	s_nop 1
	v_cndmask_b32_e32 v60, 0, v60, vcc
	v_add_u32_e32 v54, v54, v60
	v_cmp_lt_u32_e32 vcc, 5, v55
	s_nop 1
	v_cndmask_b32_e32 v61, 0, v61, vcc
	v_add_u32_e32 v54, v54, v61
	v_cmp_lt_u32_e32 vcc, 6, v55
	s_nop 1
	v_cndmask_b32_e32 v62, 0, v62, vcc
	v_add_u32_e32 v54, v54, v62
	v_cmp_lt_u32_e32 vcc, 7, v55
	s_nop 1
	v_cndmask_b32_e32 v63, 0, v63, vcc
	v_add_u32_e32 v54, v54, v63
	v_mov_b32_e32 v61, 0
	ds_read_b128 v[60:63], v61 offset:16416
	s_waitcnt lgkmcnt(0)
	v_cmp_lt_u32_e32 vcc, 8, v55
	s_nop 1
	v_cndmask_b32_e32 v60, 0, v60, vcc
	v_add_u32_e32 v54, v54, v60
	v_cmp_lt_u32_e32 vcc, 9, v55
	s_nop 1
	v_cndmask_b32_e32 v61, 0, v61, vcc
	v_add_u32_e32 v54, v54, v61
	v_cmp_lt_u32_e32 vcc, 10, v55
	s_nop 1
	v_cndmask_b32_e32 v62, 0, v62, vcc
	v_add_u32_e32 v54, v54, v62
	v_cmp_lt_u32_e32 vcc, 11, v55
	s_nop 1
	v_cndmask_b32_e32 v63, 0, v63, vcc
	v_add_u32_e32 v54, v54, v63
	v_mov_b32_e32 v61, 0
	ds_read_b128 v[60:63], v61 offset:16432
	s_waitcnt lgkmcnt(0)
	v_cmp_lt_u32_e32 vcc, 12, v55
	s_nop 1
	v_cndmask_b32_e32 v60, 0, v60, vcc
	v_add_u32_e32 v54, v54, v60
	v_cmp_lt_u32_e32 vcc, 13, v55
	s_nop 1
	v_cndmask_b32_e32 v61, 0, v61, vcc
	v_add_u32_e32 v54, v54, v61
	v_cmp_lt_u32_e32 vcc, 14, v55
	s_nop 1
	v_cndmask_b32_e32 v62, 0, v62, vcc
	v_add_u32_e32 v54, v54, v62
	v_mov_b32_e32 v62, v54
	v_sub_u32_e32 v59, v59, v58
	v_add_u32_e32 v59, v59, v62
	v_add_u32_e32 v60, v59, v50
	v_add_u32_e32 v61, v59, v56
	v_add_u32_e32 v62, v59, v57
	v_mov_b32_e32 v50, v59
	v_mov_b32_e32 v51, v60
	v_mov_b32_e32 v52, v61
	v_mov_b32_e32 v53, v62
	ds_write_b128 v1, v[50:53]
	v_and_b32_e32 v56, 7, v0
	v_lshrrev_b32_e32 v57, 3, v0
	v_lshl_add_u32 v57, s42, 7, v57
	v_cmp_eq_u32_e32 vcc, 0, v56
	v_cmp_gt_i32_e64 s[4:5], s44, v57
	s_and_b64 s[4:5], vcc, s[4:5]
	v_add_u32_e32 v58, s36, v59
	v_lshlrev_b32_e32 v56, 2, v57
	s_and_saveexec_b64 s[10:11], s[4:5]
	global_store_dword v56, v58, s[38:39]
	s_add_i32 s7, s44, -1
	v_cmp_eq_u32_e32 vcc, s7, v57
	s_and_b64 exec, exec, vcc
	v_mov_b32_e32 v58, s45
	global_store_dword v56, v58, s[38:39] offset:4
	s_mov_b64 exec, s[10:11]
	s_waitcnt lgkmcnt(0)
	s_barrier
	v_lshrrev_b32_e32 v54, 25, v2
	v_bfe_u32 v55, v2, 13, 12
	v_min_u32_e32 v55, 31, v55
	v_xor_b32_e32 v55, s8, v55
	v_lshl_or_b32 v54, v54, 5, v55
	v_lshlrev_b32_e32 v56, 2, v54
	ds_read_b32 v56, v56
	v_lshrrev_b32_e32 v54, 25, v4
	v_bfe_u32 v55, v4, 13, 12
	v_min_u32_e32 v55, 31, v55
	v_xor_b32_e32 v55, s8, v55
	v_lshl_or_b32 v54, v54, 5, v55
	v_lshlrev_b32_e32 v57, 2, v54
	ds_read_b32 v57, v57
	v_lshrrev_b32_e32 v54, 25, v6
	v_bfe_u32 v55, v6, 13, 12
	v_min_u32_e32 v55, 31, v55
	v_xor_b32_e32 v55, s8, v55
	v_lshl_or_b32 v54, v54, 5, v55
	v_lshlrev_b32_e32 v58, 2, v54
	ds_read_b32 v58, v58
	v_lshrrev_b32_e32 v54, 25, v8
	v_bfe_u32 v55, v8, 13, 12
	v_min_u32_e32 v55, 31, v55
	v_xor_b32_e32 v55, s8, v55
	v_lshl_or_b32 v54, v54, 5, v55
	v_lshlrev_b32_e32 v59, 2, v54
	ds_read_b32 v59, v59
	s_waitcnt lgkmcnt(0)
	v_add_u32_e32 v34, v34, v56
	v_and_b32_e32 v2, 0x1ffffff, v2
	v_add_u32_e32 v35, v35, v57
	v_and_b32_e32 v4, 0x1ffffff, v4
	v_add_u32_e32 v36, v36, v58
	v_and_b32_e32 v6, 0x1ffffff, v6
	v_add_u32_e32 v37, v37, v59
	v_and_b32_e32 v8, 0x1ffffff, v8
	v_lshrrev_b32_e32 v54, 25, v10
	v_bfe_u32 v55, v10, 13, 12
	v_min_u32_e32 v55, 31, v55
	v_xor_b32_e32 v55, s8, v55
	v_lshl_or_b32 v54, v54, 5, v55
	v_lshlrev_b32_e32 v56, 2, v54
	ds_read_b32 v56, v56
	v_lshrrev_b32_e32 v54, 25, v12
	v_bfe_u32 v55, v12, 13, 12
	v_min_u32_e32 v55, 31, v55
	v_xor_b32_e32 v55, s8, v55
	v_lshl_or_b32 v54, v54, 5, v55
	v_lshlrev_b32_e32 v57, 2, v54
	ds_read_b32 v57, v57
	v_lshrrev_b32_e32 v54, 25, v14
	v_bfe_u32 v55, v14, 13, 12
	v_min_u32_e32 v55, 31, v55
	v_xor_b32_e32 v55, s8, v55
	v_lshl_or_b32 v54, v54, 5, v55
	v_lshlrev_b32_e32 v58, 2, v54
	ds_read_b32 v58, v58
	v_lshrrev_b32_e32 v54, 25, v16
	v_bfe_u32 v55, v16, 13, 12
	v_min_u32_e32 v55, 31, v55
	v_xor_b32_e32 v55, s8, v55
	v_lshl_or_b32 v54, v54, 5, v55
	v_lshlrev_b32_e32 v59, 2, v54
	ds_read_b32 v59, v59
	s_waitcnt lgkmcnt(0)
	v_add_u32_e32 v38, v38, v56
	v_and_b32_e32 v10, 0x1ffffff, v10
	v_add_u32_e32 v39, v39, v57
	v_and_b32_e32 v12, 0x1ffffff, v12
	v_add_u32_e32 v40, v40, v58
	v_and_b32_e32 v14, 0x1ffffff, v14
	v_add_u32_e32 v41, v41, v59
	v_and_b32_e32 v16, 0x1ffffff, v16
	v_lshrrev_b32_e32 v54, 25, v18
	v_bfe_u32 v55, v18, 13, 12
	v_min_u32_e32 v55, 31, v55
	v_xor_b32_e32 v55, s8, v55
	v_lshl_or_b32 v54, v54, 5, v55
	v_lshlrev_b32_e32 v56, 2, v54
	ds_read_b32 v56, v56
	v_lshrrev_b32_e32 v54, 25, v20
	v_bfe_u32 v55, v20, 13, 12
	v_min_u32_e32 v55, 31, v55
	v_xor_b32_e32 v55, s8, v55
	v_lshl_or_b32 v54, v54, 5, v55
	v_lshlrev_b32_e32 v57, 2, v54
	ds_read_b32 v57, v57
	v_lshrrev_b32_e32 v54, 25, v22
	v_bfe_u32 v55, v22, 13, 12
	v_min_u32_e32 v55, 31, v55
	v_xor_b32_e32 v55, s8, v55
	v_lshl_or_b32 v54, v54, 5, v55
	v_lshlrev_b32_e32 v58, 2, v54
	ds_read_b32 v58, v58
	v_lshrrev_b32_e32 v54, 25, v24
	v_bfe_u32 v55, v24, 13, 12
	v_min_u32_e32 v55, 31, v55
	v_xor_b32_e32 v55, s8, v55
	v_lshl_or_b32 v54, v54, 5, v55
	v_lshlrev_b32_e32 v59, 2, v54
	ds_read_b32 v59, v59
	s_waitcnt lgkmcnt(0)
	v_add_u32_e32 v42, v42, v56
	v_and_b32_e32 v18, 0x1ffffff, v18
	v_add_u32_e32 v43, v43, v57
	v_and_b32_e32 v20, 0x1ffffff, v20
	v_add_u32_e32 v44, v44, v58
	v_and_b32_e32 v22, 0x1ffffff, v22
	v_add_u32_e32 v45, v45, v59
	v_and_b32_e32 v24, 0x1ffffff, v24
	v_lshrrev_b32_e32 v54, 25, v26
	v_bfe_u32 v55, v26, 13, 12
	v_min_u32_e32 v55, 31, v55
	v_xor_b32_e32 v55, s8, v55
	v_lshl_or_b32 v54, v54, 5, v55
	v_lshlrev_b32_e32 v56, 2, v54
	ds_read_b32 v56, v56
	v_lshrrev_b32_e32 v54, 25, v28
	v_bfe_u32 v55, v28, 13, 12
	v_min_u32_e32 v55, 31, v55
	v_xor_b32_e32 v55, s8, v55
	v_lshl_or_b32 v54, v54, 5, v55
	v_lshlrev_b32_e32 v57, 2, v54
	ds_read_b32 v57, v57
	v_lshrrev_b32_e32 v54, 25, v30
	v_bfe_u32 v55, v30, 13, 12
	v_min_u32_e32 v55, 31, v55
	v_xor_b32_e32 v55, s8, v55
	v_lshl_or_b32 v54, v54, 5, v55
	v_lshlrev_b32_e32 v58, 2, v54
	ds_read_b32 v58, v58
	v_lshrrev_b32_e32 v54, 25, v32
	v_bfe_u32 v55, v32, 13, 12
	v_min_u32_e32 v55, 31, v55
	v_xor_b32_e32 v55, s8, v55
	v_lshl_or_b32 v54, v54, 5, v55
	v_lshlrev_b32_e32 v59, 2, v54
	ds_read_b32 v59, v59
	s_waitcnt lgkmcnt(0)
	v_add_u32_e32 v46, v46, v56
	v_and_b32_e32 v26, 0x1ffffff, v26
	v_add_u32_e32 v47, v47, v57
	v_and_b32_e32 v28, 0x1ffffff, v28
	v_add_u32_e32 v48, v48, v58
	v_and_b32_e32 v30, 0x1ffffff, v30
	v_add_u32_e32 v49, v49, v59
	v_and_b32_e32 v32, 0x1ffffff, v32
	s_movk_i32 s14, 8000
	v_add_u32_e32 v54, 0, v0
	v_lshl_add_u32 v54, v54, 1, 0
	v_cmp_gt_i32_e32 vcc, s33, v54
	v_mov_b32_e32 v56, v34
	v_cmp_gt_u32_e64 s[4:5], s14, v56
	s_and_b64 vcc, vcc, s[4:5]
	v_lshlrev_b32_e32 v56, 3, v56
	s_and_saveexec_b64 s[4:5], vcc
	ds_write_b64 v56, v[2:3] offset:16448
	s_or_b64 exec, exec, s[4:5]
	v_add_u32_e32 v54, 0, v0
	v_lshl_add_u32 v54, v54, 1, 1
	v_cmp_gt_i32_e32 vcc, s33, v54
	v_mov_b32_e32 v56, v35
	v_cmp_gt_u32_e64 s[4:5], s14, v56
	s_and_b64 vcc, vcc, s[4:5]
	v_lshlrev_b32_e32 v56, 3, v56
	s_and_saveexec_b64 s[4:5], vcc
	ds_write_b64 v56, v[4:5] offset:16448
	s_or_b64 exec, exec, s[4:5]
	v_add_u32_e32 v54, 1024, v0
	v_lshl_add_u32 v54, v54, 1, 0
	v_cmp_gt_i32_e32 vcc, s33, v54
	v_mov_b32_e32 v56, v36
	v_cmp_gt_u32_e64 s[4:5], s14, v56
	s_and_b64 vcc, vcc, s[4:5]
	v_lshlrev_b32_e32 v56, 3, v56
	s_and_saveexec_b64 s[4:5], vcc
	ds_write_b64 v56, v[6:7] offset:16448
	s_or_b64 exec, exec, s[4:5]
	v_add_u32_e32 v54, 1024, v0
	v_lshl_add_u32 v54, v54, 1, 1
	v_cmp_gt_i32_e32 vcc, s33, v54
	v_mov_b32_e32 v56, v37
	v_cmp_gt_u32_e64 s[4:5], s14, v56
	s_and_b64 vcc, vcc, s[4:5]
	v_lshlrev_b32_e32 v56, 3, v56
	s_and_saveexec_b64 s[4:5], vcc
	ds_write_b64 v56, v[8:9] offset:16448
	s_or_b64 exec, exec, s[4:5]
	v_add_u32_e32 v54, 2048, v0
	v_lshl_add_u32 v54, v54, 1, 0
	v_cmp_gt_i32_e32 vcc, s33, v54
	v_mov_b32_e32 v56, v38
	v_cmp_gt_u32_e64 s[4:5], s14, v56
	s_and_b64 vcc, vcc, s[4:5]
	v_lshlrev_b32_e32 v56, 3, v56
	s_and_saveexec_b64 s[4:5], vcc
	ds_write_b64 v56, v[10:11] offset:16448
	s_or_b64 exec, exec, s[4:5]
	v_add_u32_e32 v54, 2048, v0
	v_lshl_add_u32 v54, v54, 1, 1
	v_cmp_gt_i32_e32 vcc, s33, v54
	v_mov_b32_e32 v56, v39
	v_cmp_gt_u32_e64 s[4:5], s14, v56
	s_and_b64 vcc, vcc, s[4:5]
	v_lshlrev_b32_e32 v56, 3, v56
	s_and_saveexec_b64 s[4:5], vcc
	ds_write_b64 v56, v[12:13] offset:16448
	s_or_b64 exec, exec, s[4:5]
	v_add_u32_e32 v54, 3072, v0
	v_lshl_add_u32 v54, v54, 1, 0
	v_cmp_gt_i32_e32 vcc, s33, v54
	v_mov_b32_e32 v56, v40
	v_cmp_gt_u32_e64 s[4:5], s14, v56
	s_and_b64 vcc, vcc, s[4:5]
	v_lshlrev_b32_e32 v56, 3, v56
	s_and_saveexec_b64 s[4:5], vcc
	ds_write_b64 v56, v[14:15] offset:16448
	s_or_b64 exec, exec, s[4:5]
	v_add_u32_e32 v54, 3072, v0
	v_lshl_add_u32 v54, v54, 1, 1
	v_cmp_gt_i32_e32 vcc, s33, v54
	v_mov_b32_e32 v56, v41
	v_cmp_gt_u32_e64 s[4:5], s14, v56
	s_and_b64 vcc, vcc, s[4:5]
	v_lshlrev_b32_e32 v56, 3, v56
	s_and_saveexec_b64 s[4:5], vcc
	ds_write_b64 v56, v[16:17] offset:16448
	s_or_b64 exec, exec, s[4:5]
	v_add_u32_e32 v54, 4096, v0
	v_lshl_add_u32 v54, v54, 1, 0
	v_cmp_gt_i32_e32 vcc, s33, v54
	v_mov_b32_e32 v56, v42
	v_cmp_gt_u32_e64 s[4:5], s14, v56
	s_and_b64 vcc, vcc, s[4:5]
	v_lshlrev_b32_e32 v56, 3, v56
	s_and_saveexec_b64 s[4:5], vcc
	ds_write_b64 v56, v[18:19] offset:16448
	s_or_b64 exec, exec, s[4:5]
	v_add_u32_e32 v54, 4096, v0
	v_lshl_add_u32 v54, v54, 1, 1
	v_cmp_gt_i32_e32 vcc, s33, v54
	v_mov_b32_e32 v56, v43
	v_cmp_gt_u32_e64 s[4:5], s14, v56
	s_and_b64 vcc, vcc, s[4:5]
	v_lshlrev_b32_e32 v56, 3, v56
	s_and_saveexec_b64 s[4:5], vcc
	ds_write_b64 v56, v[20:21] offset:16448
	s_or_b64 exec, exec, s[4:5]
	v_add_u32_e32 v54, 5120, v0
	v_lshl_add_u32 v54, v54, 1, 0
	v_cmp_gt_i32_e32 vcc, s33, v54
	v_mov_b32_e32 v56, v44
	v_cmp_gt_u32_e64 s[4:5], s14, v56
	s_and_b64 vcc, vcc, s[4:5]
	v_lshlrev_b32_e32 v56, 3, v56
	s_and_saveexec_b64 s[4:5], vcc
	ds_write_b64 v56, v[22:23] offset:16448
	s_or_b64 exec, exec, s[4:5]
	v_add_u32_e32 v54, 5120, v0
	v_lshl_add_u32 v54, v54, 1, 1
	v_cmp_gt_i32_e32 vcc, s33, v54
	v_mov_b32_e32 v56, v45
	v_cmp_gt_u32_e64 s[4:5], s14, v56
	s_and_b64 vcc, vcc, s[4:5]
	v_lshlrev_b32_e32 v56, 3, v56
	s_and_saveexec_b64 s[4:5], vcc
	ds_write_b64 v56, v[24:25] offset:16448
	s_or_b64 exec, exec, s[4:5]
	v_add_u32_e32 v54, 6144, v0
	v_lshl_add_u32 v54, v54, 1, 0
	v_cmp_gt_i32_e32 vcc, s33, v54
	v_mov_b32_e32 v56, v46
	v_cmp_gt_u32_e64 s[4:5], s14, v56
	s_and_b64 vcc, vcc, s[4:5]
	v_lshlrev_b32_e32 v56, 3, v56
	s_and_saveexec_b64 s[4:5], vcc
	ds_write_b64 v56, v[26:27] offset:16448
	s_or_b64 exec, exec, s[4:5]
	v_add_u32_e32 v54, 6144, v0
	v_lshl_add_u32 v54, v54, 1, 1
	v_cmp_gt_i32_e32 vcc, s33, v54
	v_mov_b32_e32 v56, v47
	v_cmp_gt_u32_e64 s[4:5], s14, v56
	s_and_b64 vcc, vcc, s[4:5]
	v_lshlrev_b32_e32 v56, 3, v56
	s_and_saveexec_b64 s[4:5], vcc
	ds_write_b64 v56, v[28:29] offset:16448
	s_or_b64 exec, exec, s[4:5]
	v_add_u32_e32 v54, 7168, v0
	v_lshl_add_u32 v54, v54, 1, 0
	v_cmp_gt_i32_e32 vcc, s33, v54
	v_mov_b32_e32 v56, v48
	v_cmp_gt_u32_e64 s[4:5], s14, v56
	s_and_b64 vcc, vcc, s[4:5]
	v_lshlrev_b32_e32 v56, 3, v56
	s_and_saveexec_b64 s[4:5], vcc
	ds_write_b64 v56, v[30:31] offset:16448
	s_or_b64 exec, exec, s[4:5]
	v_add_u32_e32 v54, 7168, v0
	v_lshl_add_u32 v54, v54, 1, 1
	v_cmp_gt_i32_e32 vcc, s33, v54
	v_mov_b32_e32 v56, v49
	v_cmp_gt_u32_e64 s[4:5], s14, v56
	s_and_b64 vcc, vcc, s[4:5]
	v_lshlrev_b32_e32 v56, 3, v56
	s_and_saveexec_b64 s[4:5], vcc
	ds_write_b64 v56, v[32:33] offset:16448
	s_or_b64 exec, exec, s[4:5]
	s_waitcnt lgkmcnt(0)
	s_barrier
	s_sub_i32 s6, s33, 0
	s_min_i32 s6, s6, 8000
	v_lshlrev_b32_e32 v59, 1, v0
	v_cmp_gt_i32_e32 vcc, s6, v59
	s_and_saveexec_b64 s[10:11], vcc
	s_cbranch_execz .Ll2_cpdone0
	v_add_u32_e32 v56, s36, v59
	v_ashrrev_i32_e32 v57, 31, v56
	v_lshl_add_u64 v[56:57], v[56:57], 3, s[40:41]
	v_lshlrev_b32_e32 v58, 4, v0
	s_mov_b64 s[4:5], 0
	s_mov_b64 s[12:13], 0x4000

.LBB6_36:
	s_or_b64 exec, exec, s[22:23]
	s_mov_b64 s[2:3], s[42:43]
	s_mov_b64 s[20:21], s[44:45]
	s_mov_b64 s[4:5], s[48:49]
	s_mov_b64 s[6:7], s[50:51]
	s_mov_b64 s[22:23], s[52:53]
	v_cndmask_b32_e32 v8, 0, v16, vcc
	v_ashrrev_i32_e32 v9, 31, v8
	v_lshlrev_b64 v[0:1], 8, v[8:9]
	v_mov_b32_e32 v5, 0
	s_waitcnt lgkmcnt(0)
	v_lshl_add_u64 v[0:1], s[22:23], 0, v[0:1]
	v_lshlrev_b32_e32 v4, 1, v18
	v_lshl_add_u64 v[0:1], v[0:1], 0, v[4:5]
	global_load_dwordx4 v[0:3], v[0:1], off nt
	v_mul_f32_e32 v4, v33, v33
	v_fmac_f32_e32 v4, v32, v32
	v_fmac_f32_e32 v4, v30, v30
	v_fmac_f32_e32 v4, v31, v31
	v_xor_b32_e32 v6, 1, v19
	v_fmac_f32_e32 v4, v26, v26
	v_cmp_lt_i32_e64 s[0:1], v6, v51
	v_fmac_f32_e32 v4, v27, v27
	v_fmac_f32_e32 v4, v28, v28
	v_cndmask_b32_e64 v6, v19, v6, s[0:1]
	v_lshlrev_b32_e32 v6, 2, v6
	v_fmac_f32_e32 v4, v29, v29
	ds_bpermute_b32 v12, v6, v4
	v_xor_b32_e32 v7, 2, v19
	v_cmp_lt_i32_e64 s[0:1], v7, v51
	v_xor_b32_e32 v10, 4, v19
	v_xor_b32_e32 v11, 8, v19
	s_waitcnt vmcnt(0)
	v_fma_mix_f32 v13, v32, v0, 0 op_sel_hi:[0,1,0]
	v_fma_mix_f32 v0, v33, v0, v13 op_sel:[0,1,0] op_sel_hi:[0,1,0]
	v_fma_mix_f32 v0, v30, v1, v0 op_sel_hi:[0,1,0]
	v_fma_mix_f32 v0, v31, v1, v0 op_sel:[0,1,0] op_sel_hi:[0,1,0]
	v_fma_mix_f32 v0, v26, v2, v0 op_sel_hi:[0,1,0]
	v_fma_mix_f32 v0, v27, v2, v0 op_sel:[0,1,0] op_sel_hi:[0,1,0]
	v_fma_mix_f32 v0, v28, v3, v0 op_sel_hi:[0,1,0]
	v_fma_mix_f32 v0, v29, v3, v0 op_sel:[0,1,0] op_sel_hi:[0,1,0]
	ds_bpermute_b32 v1, v6, v0
	v_cndmask_b32_e64 v2, v19, v7, s[0:1]
	v_lshlrev_b32_e32 v2, 2, v2
	s_waitcnt lgkmcnt(1)
	v_add_f32_e32 v3, v4, v12
	ds_bpermute_b32 v4, v2, v3
	s_waitcnt lgkmcnt(1)
	v_add_f32_e32 v0, v0, v1
	ds_bpermute_b32 v1, v2, v0
	v_cmp_lt_i32_e64 s[0:1], v10, v51
	s_waitcnt lgkmcnt(1)
	v_add_f32_e32 v3, v3, v4
	v_cndmask_b32_e64 v2, v19, v10, s[0:1]
	v_lshlrev_b32_e32 v2, 2, v2
	s_waitcnt lgkmcnt(0)
	v_add_f32_e32 v0, v0, v1
	ds_bpermute_b32 v4, v2, v3
	ds_bpermute_b32 v1, v2, v0
	v_cmp_lt_i32_e64 s[0:1], v11, v51
	s_waitcnt lgkmcnt(1)
	v_add_f32_e32 v10, v3, v4
	v_cndmask_b32_e64 v2, v19, v11, s[0:1]
	v_lshlrev_b32_e32 v2, 2, v2
	s_waitcnt lgkmcnt(0)
	v_add_f32_e32 v11, v0, v1
	ds_bpermute_b32 v12, v2, v11
	ds_bpermute_b32 v13, v2, v10
	s_and_saveexec_b64 s[0:1], vcc
	s_cbranch_execz .LBB6_38
	v_ashrrev_i32_e32 v0, 5, v50
	v_ashrrev_i32_e32 v1, 31, v0
	v_lshl_add_u64 v[0:1], v[0:1], 2, s[12:13]
	global_load_dword v6, v[0:1], off
	v_lshl_add_u64 v[0:1], v[8:9], 2, s[14:15]
	global_load_dword v7, v[0:1], off
	v_lshlrev_b64 v[0:1], 7, v[16:17]
	v_mov_b32_e32 v19, v5
	v_lshl_add_u64 v[2:3], s[20:21], 0, v[0:1]
	v_lshl_add_u64 v[2:3], v[2:3], 0, v[18:19]
	global_load_dwordx2 v[14:15], v[2:3], off nt
	v_lshl_add_u64 v[0:1], s[2:3], 0, v[0:1]
	v_lshlrev_b64 v[2:3], 8, v[16:17]
	v_lshl_add_u64 v[0:1], v[0:1], 0, v[18:19]
	global_load_dwordx2 v[20:21], v[0:1], off nt
	v_lshl_add_u64 v[0:1], s[6:7], 0, v[2:3]
	v_lshlrev_b32_e32 v4, 1, v18
	v_lshl_add_u64 v[0:1], v[0:1], 0, v[4:5]
	global_load_dwordx4 v[0:3], v[0:1], off nt
	s_waitcnt lgkmcnt(0)
	v_add_f32_e32 v4, v10, v13
	s_mov_b32 s2, 0xf800000
	s_ashr_i32 s17, s16, 31
	v_mul_f32_e32 v13, 0x4f800000, v4
	v_cmp_gt_f32_e32 vcc, s2, v4
	s_lshl_b64 s[0:1], s[16:17], 2
	s_add_u32 s2, s10, s0
	v_cndmask_b32_e32 v13, v4, v13, vcc
	v_sqrt_f32_e32 v4, v13
	v_lshlrev_b64 v[8:9], 9, v[16:17]
	s_addc_u32 s3, s11, s1
	v_lshl_add_u64 v[8:9], s[4:5], 0, v[8:9]
	s_load_dword s5, s[2:3], 0x0
	s_add_u32 s2, s18, s0
	s_addc_u32 s3, s19, s1
	s_add_u32 s0, s8, s0
	v_add_u32_e32 v16, -1, v4
	v_add_u32_e32 v17, 1, v4
	s_addc_u32 s1, s9, s1
	v_fma_f32 v19, -v16, v4, v13
	s_load_dword s4, s[2:3], 0x0
	v_fma_f32 v22, -v17, v4, v13
	s_load_dword s2, s[0:1], 0x0
	v_cmp_ge_f32_e64 s[0:1], 0, v19
	v_add_f32_e32 v12, v11, v12
	v_mov_b32_e32 v11, 0x43800000
	v_cndmask_b32_e64 v16, v4, v16, s[0:1]
	v_cmp_lt_f32_e64 s[0:1], 0, v22
	s_waitcnt lgkmcnt(0)
	v_mul_f32_e32 v4, s5, v11
	v_mov_b32_e32 v10, 0x260
	v_cndmask_b32_e64 v11, v16, v17, s[0:1]
	v_mul_f32_e32 v16, 0x37800000, v11
	v_cndmask_b32_e32 v11, v11, v16, vcc
	v_cmp_class_f32_e32 vcc, v13, v10
	s_waitcnt vmcnt(2)
	v_cvt_pk_f32_fp8_e32 v[22:23], v14
	v_cndmask_b32_e32 v10, v11, v13, vcc
	v_max_f32_e32 v13, 0x322bcc77, v10
	v_pk_mul_f32 v[10:11], v[6:7], v[12:13]
	v_cvt_pk_f32_fp8_e32 v[34:35], v15
	v_div_scale_f32 v19, s[0:1], v11, v11, v10
	v_rcp_f32_e32 v45, v19
	v_cvt_pk_f32_fp8_sdwa v[24:25], v14 src0_sel:WORD_1
	v_cvt_pk_f32_fp8_sdwa v[36:37], v15 src0_sel:WORD_1
	s_waitcnt vmcnt(1)
	v_cvt_pk_f32_fp8_e32 v[12:13], v20
	v_cvt_pk_f32_fp8_sdwa v[14:15], v20 src0_sel:WORD_1
	v_cvt_pk_f32_fp8_e32 v[16:17], v21
	v_cvt_pk_f32_fp8_sdwa v[6:7], v21 src0_sel:WORD_1
	s_waitcnt vmcnt(0)
	v_cvt_f32_f16_e32 v20, v0
	v_cvt_f32_f16_sdwa v21, v0 dst_sel:DWORD dst_unused:UNUSED_PAD src0_sel:WORD_1
	v_cvt_f32_f16_e32 v38, v1
	v_cvt_f32_f16_sdwa v39, v1 dst_sel:DWORD dst_unused:UNUSED_PAD src0_sel:WORD_1
	v_pk_mul_f32 v[0:1], s[4:5], v[22:23] op_sel_hi:[0,1]
	v_pk_mul_f32 v[22:23], s[4:5], v[34:35] op_sel_hi:[0,1]
	v_fma_f32 v34, -v19, v45, 1.0
	v_div_scale_f32 v44, vcc, v10, v11, v10
	v_fmac_f32_e32 v45, v34, v45
	v_mul_f32_e32 v34, v44, v45
	v_fma_f32 v35, -v19, v34, v44
	v_fmac_f32_e32 v34, v35, v45
	v_fma_f32 v19, -v19, v34, v44
	v_cvt_f32_f16_e32 v40, v2
	v_cvt_f32_f16_sdwa v41, v2 dst_sel:DWORD dst_unused:UNUSED_PAD src0_sel:WORD_1
	v_cvt_f32_f16_e32 v42, v3
	v_cvt_f32_f16_sdwa v43, v3 dst_sel:DWORD dst_unused:UNUSED_PAD src0_sel:WORD_1
	v_div_fmas_f32 v19, v19, v45, v34
	v_pk_mul_f32 v[2:3], s[4:5], v[24:25] op_sel_hi:[0,1]
	v_pk_mul_f32 v[24:25], s[4:5], v[36:37] op_sel_hi:[0,1]
	v_div_fixup_f32 v10, v19, v11, v10
	v_pk_fma_f32 v[0:1], v[10:11], v[32:33], v[0:1] op_sel_hi:[0,1,1]
	v_pk_fma_f32 v[2:3], v[10:11], v[30:31], v[2:3] op_sel_hi:[0,1,1]
	v_pk_fma_f32 v[22:23], v[10:11], v[26:27], v[22:23] op_sel_hi:[0,1,1]
	v_pk_fma_f32 v[24:25], v[10:11], v[28:29], v[24:25] op_sel_hi:[0,1,1]
	v_pk_fma_f32 v[0:1], s[2:3], v[12:13], v[0:1] op_sel_hi:[0,1,1]
	v_pk_fma_f32 v[2:3], s[2:3], v[14:15], v[2:3] op_sel_hi:[0,1,1]
	v_pk_fma_f32 v[10:11], s[2:3], v[16:17], v[22:23] op_sel_hi:[0,1,1]
	v_pk_fma_f32 v[6:7], s[2:3], v[6:7], v[24:25] op_sel_hi:[0,1,1]
	v_pk_fma_f32 v[0:1], v[4:5], v[20:21], v[0:1] op_sel_hi:[0,1,1]
	v_pk_fma_f32 v[2:3], v[4:5], v[38:39], v[2:3] op_sel_hi:[0,1,1]
	v_pk_fma_f32 v[10:11], v[4:5], v[40:41], v[10:11] op_sel_hi:[0,1,1]
	v_pk_fma_f32 v[12:13], v[4:5], v[42:43], v[6:7] op_sel_hi:[0,1,1]
	v_lshlrev_b32_e32 v4, 2, v18
	v_lshl_add_u64 v[4:5], v[8:9], 0, v[4:5]
	global_store_dwordx4 v[4:5], v[0:3], off nt
	global_store_dwordx4 v[4:5], v[10:13], off offset:16 nt
